# banded attention (dilation 1 and 4): QK K-fragment LDS reads rotated through four buffers, four reads in flight instead of read-wait-MFMA
# speedup vs baseline: 1.0146x; 1.0146x over previous
.LBB0_458:
	s_and_b32 s81, s8, 1
	s_add_i32 s8, s79, 0xffffff81
	v_cmp_le_i32_e32 vcc, s8, v177
	v_cmp_ge_i32_e64 s[8:9], s79, v175
	s_and_b64 s[30:31], vcc, s[8:9]
	s_and_saveexec_b64 s[8:9], s[30:31]
	s_cbranch_execz .LBB0_465
	s_lshl_b32 s82, s81, 14
	s_add_i32 s30, s82, 0
	v_add3_u32 v2, s30, v200, v199
	ds_read_b128 v[4:7], v2 offset:32768
	ds_read_b128 v[224:227], v2 offset:40960
	v_add3_u32 v2, s30, v201, v199
	ds_read_b128 v[228:231], v2 offset:32768
	ds_read_b128 v[232:235], v2 offset:40960
	v_add_u32_e32 v11, 50, v179
	v_add_u32_e32 v13, 49, v179
	v_add_u32_e32 v15, 48, v179
	v_add_u32_e32 v17, 43, v179
	s_waitcnt lgkmcnt(3)
	v_mfma_f32_32x32x16_bf16 v[82:97], v[4:7], v[114:117], 0
	v_add3_u32 v2, s30, v202, v199
	ds_read_b128 v[4:7], v2 offset:32768
	s_waitcnt lgkmcnt(3)
	v_mfma_f32_32x32x16_bf16 v[98:113], v[224:227], v[114:117], 0
	ds_read_b128 v[224:227], v2 offset:40960
	s_waitcnt lgkmcnt(3)
	v_mfma_f32_32x32x16_bf16 v[82:97], v[228:231], v[118:121], v[82:97]
	v_add3_u32 v2, s30, v203, v199
	ds_read_b128 v[228:231], v2 offset:32768
	s_waitcnt lgkmcnt(3)
	v_mfma_f32_32x32x16_bf16 v[98:113], v[232:235], v[118:121], v[98:113]
	ds_read_b128 v[232:235], v2 offset:40960
	s_waitcnt vmcnt(5) lgkmcnt(3)
	v_mfma_f32_32x32x16_bf16 v[82:97], v[4:7], v[122:125], v[82:97]
	v_add3_u32 v2, s30, v204, v199
	ds_read_b128 v[4:7], v2 offset:32768
	s_waitcnt lgkmcnt(3)
	v_mfma_f32_32x32x16_bf16 v[98:113], v[224:227], v[122:125], v[98:113]
	ds_read_b128 v[224:227], v2 offset:40960
	s_waitcnt vmcnt(4) lgkmcnt(3)
	v_mfma_f32_32x32x16_bf16 v[82:97], v[228:231], v[126:129], v[82:97]
	v_add3_u32 v2, s30, v205, v199
	ds_read_b128 v[228:231], v2 offset:32768
	s_waitcnt lgkmcnt(3)
	v_mfma_f32_32x32x16_bf16 v[98:113], v[232:235], v[126:129], v[98:113]
	ds_read_b128 v[232:235], v2 offset:40960
	s_waitcnt vmcnt(3) lgkmcnt(3)
	v_mfma_f32_32x32x16_bf16 v[82:97], v[4:7], v[134:137], v[82:97]
	v_add3_u32 v2, s30, v206, v199
	ds_read_b128 v[4:7], v2 offset:32768
	s_waitcnt lgkmcnt(3)
	v_mfma_f32_32x32x16_bf16 v[98:113], v[224:227], v[134:137], v[98:113]
	ds_read_b128 v[224:227], v2 offset:40960
	s_waitcnt vmcnt(2) lgkmcnt(3)
	v_mfma_f32_32x32x16_bf16 v[82:97], v[228:231], v[138:141], v[82:97]
	v_add3_u32 v2, s30, v207, v199
	ds_read_b128 v[228:231], v2 offset:32768
	s_waitcnt lgkmcnt(3)
	v_mfma_f32_32x32x16_bf16 v[98:113], v[232:235], v[138:141], v[98:113]
	ds_read_b128 v[232:235], v2 offset:40960
	s_waitcnt vmcnt(1) lgkmcnt(3)
	v_mfma_f32_32x32x16_bf16 v[82:97], v[4:7], v[142:145], v[82:97]
	s_waitcnt lgkmcnt(2)
	v_mfma_f32_32x32x16_bf16 v[98:113], v[224:227], v[142:145], v[98:113]
	s_waitcnt vmcnt(0) lgkmcnt(1)
	v_mfma_f32_32x32x16_bf16 v[82:97], v[228:231], v[146:149], v[82:97]
	v_add_u32_e32 v2, 59, v179
	v_cmp_lt_u32_e32 vcc, s55, v2
	v_add_u32_e32 v2, 27, v179
	v_add_u32_e32 v4, 58, v179
	s_nop 7
	v_cndmask_b32_e32 v5, v220, v82, vcc
	s_waitcnt lgkmcnt(0)
	v_mfma_f32_32x32x16_bf16 v[98:113], v[232:235], v[146:149], v[98:113]
	v_cmp_lt_u32_e32 vcc, s55, v2
	v_add_u32_e32 v6, 57, v179
	v_add_u32_e32 v7, 56, v179
	v_add_u32_e32 v9, 51, v179
	s_nop 7
	v_cndmask_b32_e32 v2, v220, v98, vcc
	v_cmp_lt_u32_e32 vcc, s55, v4
	v_add_u32_e32 v4, 26, v179
	s_nop 0
	v_cndmask_b32_e32 v8, v220, v83, vcc
	v_cmp_lt_u32_e32 vcc, s55, v4
	s_nop 1
	v_cndmask_b32_e32 v4, v220, v99, vcc
	v_cmp_lt_u32_e32 vcc, s55, v6
	v_add_u32_e32 v6, 25, v179
	s_nop 0
	v_cndmask_b32_e32 v10, v220, v84, vcc
	v_cmp_lt_u32_e32 vcc, s55, v6
	s_nop 1
	v_cndmask_b32_e32 v6, v220, v100, vcc
	v_cmp_lt_u32_e32 vcc, s55, v7
	v_add_u32_e32 v7, 24, v179
	v_max_f32_e32 v100, v5, v5
	v_cndmask_b32_e32 v12, v220, v85, vcc
	v_cmp_lt_u32_e32 vcc, s55, v7
	s_nop 1
	v_cndmask_b32_e32 v7, v220, v101, vcc
	v_cmp_lt_u32_e32 vcc, s55, v9
	v_add_u32_e32 v9, 19, v179
	s_nop 0
	v_cndmask_b32_e32 v14, v220, v86, vcc
	v_cmp_lt_u32_e32 vcc, s55, v9
	s_nop 1
	v_cndmask_b32_e32 v9, v220, v102, vcc
	v_cmp_lt_u32_e32 vcc, s55, v11
	v_add_u32_e32 v11, 18, v179
	s_nop 0
	v_cndmask_b32_e32 v16, v220, v87, vcc
	v_cmp_lt_u32_e32 vcc, s55, v11
	s_nop 1
	v_cndmask_b32_e32 v11, v220, v103, vcc
	v_cmp_lt_u32_e32 vcc, s55, v13
	v_add_u32_e32 v13, 17, v179
	s_nop 0
	v_cndmask_b32_e32 v83, v220, v88, vcc
	v_cmp_lt_u32_e32 vcc, s55, v13
	s_nop 1
	v_cndmask_b32_e32 v13, v220, v104, vcc
	v_cmp_lt_u32_e32 vcc, s55, v15
	v_add_u32_e32 v15, 16, v179
	s_nop 0
	v_cndmask_b32_e32 v85, v220, v89, vcc
	v_cmp_lt_u32_e32 vcc, s55, v15
	s_nop 1
	v_cndmask_b32_e32 v15, v220, v105, vcc
	v_cmp_lt_u32_e32 vcc, s55, v17
	v_add_u32_e32 v17, 11, v179
	s_nop 0
	v_cndmask_b32_e32 v87, v220, v90, vcc
	v_cmp_lt_u32_e32 vcc, s55, v17
	v_add_u32_e32 v17, 42, v179
	s_nop 0
	v_cndmask_b32_e32 v82, v220, v106, vcc
	v_cmp_lt_u32_e32 vcc, s55, v17
	v_add_u32_e32 v17, 10, v179
	s_nop 0
	v_cndmask_b32_e32 v89, v220, v91, vcc
	v_cmp_lt_u32_e32 vcc, s55, v17
	v_add_u32_e32 v17, 41, v179
	s_nop 0
	v_cndmask_b32_e32 v84, v220, v107, vcc
	v_cmp_lt_u32_e32 vcc, s55, v17
	v_add_u32_e32 v17, 9, v179
	s_nop 0
	v_cndmask_b32_e32 v91, v220, v92, vcc
	v_cmp_lt_u32_e32 vcc, s55, v17
	v_add_u32_e32 v17, 40, v179
	s_nop 0
	v_cndmask_b32_e32 v86, v220, v108, vcc
	v_cmp_lt_u32_e32 vcc, s55, v17
	v_add_u32_e32 v17, 8, v179
	s_nop 0
	v_cndmask_b32_e32 v93, v220, v93, vcc
	v_cmp_lt_u32_e32 vcc, s55, v17
	v_add_u32_e32 v17, 35, v179
	s_nop 0
	v_cndmask_b32_e32 v88, v220, v109, vcc
	v_cmp_lt_u32_e32 vcc, s55, v17
	v_add_u32_e32 v17, 3, v179
	s_nop 0
	v_cndmask_b32_e32 v98, v220, v94, vcc
	v_cmp_lt_u32_e32 vcc, s55, v17
	v_add_u32_e32 v17, 34, v179
	s_nop 0
	v_cndmask_b32_e32 v90, v220, v110, vcc
	v_cmp_lt_u32_e32 vcc, s55, v17
	v_add_u32_e32 v17, 2, v179
	s_nop 0
	v_cndmask_b32_e32 v99, v220, v95, vcc
	v_cmp_lt_u32_e32 vcc, s55, v17
	v_add_u32_e32 v17, 33, v179
	s_nop 0
	v_cndmask_b32_e32 v92, v220, v111, vcc
	v_cmp_lt_u32_e32 vcc, s55, v17
	v_add_u32_e32 v17, 1, v179
	s_nop 0
	v_cndmask_b32_e32 v96, v220, v96, vcc
	v_cmp_lt_u32_e32 vcc, s55, v17
	v_add_u32_e32 v17, 32, v179
	s_nop 0
	v_cndmask_b32_e32 v94, v220, v112, vcc
	v_cmp_lt_u32_e32 vcc, s55, v17
	v_max_f32_e32 v17, v8, v8
	v_max_f32_e32 v17, v100, v17
	v_max3_f32 v17, v17, v10, v12
	v_max3_f32 v17, v17, v14, v16
	v_max3_f32 v17, v17, v83, v85
	v_max3_f32 v17, v17, v87, v89
	v_max3_f32 v17, v17, v91, v93
	v_cndmask_b32_e32 v97, v220, v97, vcc
	v_max3_f32 v17, v17, v98, v99
	v_max3_f32 v17, v17, v96, v97
	v_max3_f32 v17, v17, v2, v4
	v_max3_f32 v17, v17, v6, v7
	v_max3_f32 v17, v17, v9, v11
	v_max3_f32 v17, v17, v13, v15
	v_max3_f32 v17, v17, v82, v84
	v_cmp_lt_u32_e32 vcc, s55, v179
	v_max3_f32 v17, v17, v86, v88
	v_max3_f32 v17, v17, v90, v92
	v_cndmask_b32_e32 v95, v220, v113, vcc
	v_max3_f32 v17, v17, v94, v95
	v_mov_b32_e32 v100, v17
	s_nop 1
	v_permlane32_swap_b32_e32 v17, v100
	v_max_f32_e32 v100, v100, v100
	v_max_f32_e32 v17, v17, v17
	v_max_f32_e32 v100, v17, v100
	v_sub_f32_e32 v17, v100, v173
	v_cmp_ge_f32_e32 vcc, s56, v17
	s_cmp_eq_u64 vcc, exec
	v_mov_b32_e32 v17, 1.0
	s_cbranch_scc0 .LBB0_469
	v_cmp_gt_f32_e32 vcc, 1.0, v17
	s_cbranch_vccz .LBB0_464

.LBB0_480:
	s_and_b32 s79, s8, 1
	s_add_i32 s8, s30, 0xffffff81
	v_cmp_le_i32_e32 vcc, s8, v177
	v_cmp_ge_i32_e64 s[8:9], s30, v173
	s_and_b64 s[28:29], vcc, s[8:9]
	s_and_saveexec_b64 s[8:9], s[28:29]
	s_cbranch_execz .LBB0_487
	s_lshl_b32 s80, s79, 14
	s_add_i32 s28, s80, 0
	v_add3_u32 v2, s28, v200, v199
	ds_read_b128 v[4:7], v2 offset:32768
	ds_read_b128 v[224:227], v2 offset:40960
	v_add3_u32 v2, s28, v201, v199
	ds_read_b128 v[228:231], v2 offset:32768
	ds_read_b128 v[232:235], v2 offset:40960
	v_add_u32_e32 v11, 50, v179
	v_add_u32_e32 v13, 49, v179
	v_add_u32_e32 v15, 48, v179
	v_add_u32_e32 v17, 43, v179
	s_waitcnt lgkmcnt(3)
	v_mfma_f32_32x32x16_bf16 v[82:97], v[4:7], v[114:117], 0
	v_add3_u32 v2, s28, v202, v199
	ds_read_b128 v[4:7], v2 offset:32768
	s_waitcnt lgkmcnt(3)
	v_mfma_f32_32x32x16_bf16 v[98:113], v[224:227], v[114:117], 0
	ds_read_b128 v[224:227], v2 offset:40960
	s_waitcnt lgkmcnt(3)
	v_mfma_f32_32x32x16_bf16 v[82:97], v[228:231], v[118:121], v[82:97]
	v_add3_u32 v2, s28, v203, v199
	ds_read_b128 v[228:231], v2 offset:32768
	s_waitcnt lgkmcnt(3)
	v_mfma_f32_32x32x16_bf16 v[98:113], v[232:235], v[118:121], v[98:113]
	ds_read_b128 v[232:235], v2 offset:40960
	s_waitcnt vmcnt(5) lgkmcnt(3)
	v_mfma_f32_32x32x16_bf16 v[82:97], v[4:7], v[126:129], v[82:97]
	v_add3_u32 v2, s28, v204, v199
	ds_read_b128 v[4:7], v2 offset:32768
	s_waitcnt lgkmcnt(3)
	v_mfma_f32_32x32x16_bf16 v[98:113], v[224:227], v[126:129], v[98:113]
	ds_read_b128 v[224:227], v2 offset:40960
	s_waitcnt vmcnt(4) lgkmcnt(3)
	v_mfma_f32_32x32x16_bf16 v[82:97], v[228:231], v[130:133], v[82:97]
	v_add3_u32 v2, s28, v205, v199
	ds_read_b128 v[228:231], v2 offset:32768
	s_waitcnt lgkmcnt(3)
	v_mfma_f32_32x32x16_bf16 v[98:113], v[232:235], v[130:133], v[98:113]
	ds_read_b128 v[232:235], v2 offset:40960
	s_waitcnt vmcnt(3) lgkmcnt(3)
	v_mfma_f32_32x32x16_bf16 v[82:97], v[4:7], v[134:137], v[82:97]
	v_add3_u32 v2, s28, v206, v199
	ds_read_b128 v[4:7], v2 offset:32768
	s_waitcnt lgkmcnt(3)
	v_mfma_f32_32x32x16_bf16 v[98:113], v[224:227], v[134:137], v[98:113]
	ds_read_b128 v[224:227], v2 offset:40960
	s_waitcnt vmcnt(2) lgkmcnt(3)
	v_mfma_f32_32x32x16_bf16 v[82:97], v[228:231], v[138:141], v[82:97]
	v_add3_u32 v2, s28, v207, v199
	ds_read_b128 v[228:231], v2 offset:32768
	s_waitcnt lgkmcnt(3)
	v_mfma_f32_32x32x16_bf16 v[98:113], v[232:235], v[138:141], v[98:113]
	ds_read_b128 v[232:235], v2 offset:40960
	s_waitcnt vmcnt(1) lgkmcnt(3)
	v_mfma_f32_32x32x16_bf16 v[82:97], v[4:7], v[142:145], v[82:97]
	s_waitcnt lgkmcnt(2)
	v_mfma_f32_32x32x16_bf16 v[98:113], v[224:227], v[142:145], v[98:113]
	s_waitcnt vmcnt(0) lgkmcnt(1)
	v_mfma_f32_32x32x16_bf16 v[82:97], v[228:231], v[146:149], v[82:97]
	v_add_u32_e32 v2, 59, v179
	v_cmp_lt_u32_e32 vcc, s55, v2
	v_add_u32_e32 v2, 27, v179
	v_add_u32_e32 v4, 58, v179
	s_nop 7
	v_cndmask_b32_e32 v5, v220, v82, vcc
	s_waitcnt lgkmcnt(0)
	v_mfma_f32_32x32x16_bf16 v[98:113], v[232:235], v[146:149], v[98:113]
	v_cmp_lt_u32_e32 vcc, s55, v2
	v_add_u32_e32 v6, 57, v179
	v_add_u32_e32 v7, 56, v179
	v_add_u32_e32 v9, 51, v179
	s_nop 7
	v_cndmask_b32_e32 v2, v220, v98, vcc
	v_cmp_lt_u32_e32 vcc, s55, v4
	v_add_u32_e32 v4, 26, v179
	s_nop 0
	v_cndmask_b32_e32 v8, v220, v83, vcc
	v_cmp_lt_u32_e32 vcc, s55, v4
	s_nop 1
	v_cndmask_b32_e32 v4, v220, v99, vcc
	v_cmp_lt_u32_e32 vcc, s55, v6
	v_add_u32_e32 v6, 25, v179
	s_nop 0
	v_cndmask_b32_e32 v10, v220, v84, vcc
	v_cmp_lt_u32_e32 vcc, s55, v6
	s_nop 1
	v_cndmask_b32_e32 v6, v220, v100, vcc
	v_cmp_lt_u32_e32 vcc, s55, v7
	v_add_u32_e32 v7, 24, v179
	v_max_f32_e32 v100, v5, v5
	v_cndmask_b32_e32 v12, v220, v85, vcc
	v_cmp_lt_u32_e32 vcc, s55, v7
	s_nop 1
	v_cndmask_b32_e32 v7, v220, v101, vcc
	v_cmp_lt_u32_e32 vcc, s55, v9
	v_add_u32_e32 v9, 19, v179
	s_nop 0
	v_cndmask_b32_e32 v14, v220, v86, vcc
	v_cmp_lt_u32_e32 vcc, s55, v9
	s_nop 1
	v_cndmask_b32_e32 v9, v220, v102, vcc
	v_cmp_lt_u32_e32 vcc, s55, v11
	v_add_u32_e32 v11, 18, v179
	s_nop 0
	v_cndmask_b32_e32 v16, v220, v87, vcc
	v_cmp_lt_u32_e32 vcc, s55, v11
	s_nop 1
	v_cndmask_b32_e32 v11, v220, v103, vcc
	v_cmp_lt_u32_e32 vcc, s55, v13
	v_add_u32_e32 v13, 17, v179
	s_nop 0
	v_cndmask_b32_e32 v83, v220, v88, vcc
	v_cmp_lt_u32_e32 vcc, s55, v13
	s_nop 1
	v_cndmask_b32_e32 v13, v220, v104, vcc
	v_cmp_lt_u32_e32 vcc, s55, v15
	v_add_u32_e32 v15, 16, v179
	s_nop 0
	v_cndmask_b32_e32 v85, v220, v89, vcc
	v_cmp_lt_u32_e32 vcc, s55, v15
	s_nop 1
	v_cndmask_b32_e32 v15, v220, v105, vcc
	v_cmp_lt_u32_e32 vcc, s55, v17
	v_add_u32_e32 v17, 11, v179
	s_nop 0
	v_cndmask_b32_e32 v87, v220, v90, vcc
	v_cmp_lt_u32_e32 vcc, s55, v17
	v_add_u32_e32 v17, 42, v179
	s_nop 0
	v_cndmask_b32_e32 v82, v220, v106, vcc
	v_cmp_lt_u32_e32 vcc, s55, v17
	v_add_u32_e32 v17, 10, v179
	s_nop 0
	v_cndmask_b32_e32 v89, v220, v91, vcc
	v_cmp_lt_u32_e32 vcc, s55, v17
	v_add_u32_e32 v17, 41, v179
	s_nop 0
	v_cndmask_b32_e32 v84, v220, v107, vcc
	v_cmp_lt_u32_e32 vcc, s55, v17
	v_add_u32_e32 v17, 9, v179
	s_nop 0
	v_cndmask_b32_e32 v91, v220, v92, vcc
	v_cmp_lt_u32_e32 vcc, s55, v17
	v_add_u32_e32 v17, 40, v179
	s_nop 0
	v_cndmask_b32_e32 v86, v220, v108, vcc
	v_cmp_lt_u32_e32 vcc, s55, v17
	v_add_u32_e32 v17, 8, v179
	s_nop 0
	v_cndmask_b32_e32 v93, v220, v93, vcc
	v_cmp_lt_u32_e32 vcc, s55, v17
	v_add_u32_e32 v17, 35, v179
	s_nop 0
	v_cndmask_b32_e32 v88, v220, v109, vcc
	v_cmp_lt_u32_e32 vcc, s55, v17
	v_add_u32_e32 v17, 3, v179
	s_nop 0
	v_cndmask_b32_e32 v98, v220, v94, vcc
	v_cmp_lt_u32_e32 vcc, s55, v17
	v_add_u32_e32 v17, 34, v179
	s_nop 0
	v_cndmask_b32_e32 v90, v220, v110, vcc
	v_cmp_lt_u32_e32 vcc, s55, v17
	v_add_u32_e32 v17, 2, v179
	s_nop 0
	v_cndmask_b32_e32 v99, v220, v95, vcc
	v_cmp_lt_u32_e32 vcc, s55, v17
	v_add_u32_e32 v17, 33, v179
	s_nop 0
	v_cndmask_b32_e32 v92, v220, v111, vcc
	v_cmp_lt_u32_e32 vcc, s55, v17
	v_add_u32_e32 v17, 1, v179
	s_nop 0
	v_cndmask_b32_e32 v96, v220, v96, vcc
	v_cmp_lt_u32_e32 vcc, s55, v17
	v_add_u32_e32 v17, 32, v179
	s_nop 0
	v_cndmask_b32_e32 v94, v220, v112, vcc
	v_cmp_lt_u32_e32 vcc, s55, v17
	v_max_f32_e32 v17, v8, v8
	v_max_f32_e32 v17, v100, v17
	v_max3_f32 v17, v17, v10, v12
	v_max3_f32 v17, v17, v14, v16
	v_max3_f32 v17, v17, v83, v85
	v_max3_f32 v17, v17, v87, v89
	v_max3_f32 v17, v17, v91, v93
	v_cndmask_b32_e32 v97, v220, v97, vcc
	v_max3_f32 v17, v17, v98, v99
	v_max3_f32 v17, v17, v96, v97
	v_max3_f32 v17, v17, v2, v4
	v_max3_f32 v17, v17, v6, v7
	v_max3_f32 v17, v17, v9, v11
	v_max3_f32 v17, v17, v13, v15
	v_max3_f32 v17, v17, v82, v84
	v_cmp_lt_u32_e32 vcc, s55, v179
	v_max3_f32 v17, v17, v86, v88
	v_max3_f32 v17, v17, v90, v92
	v_cndmask_b32_e32 v95, v220, v113, vcc
	v_max3_f32 v17, v17, v94, v95
	v_mov_b32_e32 v100, v17
	s_nop 1
	v_permlane32_swap_b32_e32 v17, v100
	v_max_f32_e32 v100, v100, v100
	v_max_f32_e32 v17, v17, v17
	v_max_f32_e32 v100, v17, v100
	v_sub_f32_e32 v17, v100, v175
	v_cmp_ge_f32_e32 vcc, s56, v17
	s_cmp_eq_u64 vcc, exec
	v_mov_b32_e32 v17, 1.0
	s_cbranch_scc0 .LBB0_491
	v_cmp_gt_f32_e32 vcc, 1.0, v17
	s_cbranch_vccz .LBB0_486
